# g1 + phase G chunk loads as global_load with counted vmcnt waits (double buffer restored)
# speedup vs baseline: 1.0232x; 1.0012x over previous
.LBB0_2910:
	s_or_b64 exec, exec, s[20:21]
	v_readlane_b32 s20, v2, 0
	s_ashr_i32 s21, s20, 31
	s_lshl_b64 s[20:21], s[20:21], 11
	v_lshl_add_u64 v[30:31], v[14:15], 0, s[20:21]
	v_readlane_b32 s20, v2, 1
	s_ashr_i32 s21, s20, 31
	s_lshl_b64 s[20:21], s[20:21], 11
	v_lshl_add_u64 v[34:35], v[14:15], 0, s[20:21]
	v_readlane_b32 s20, v2, 2
	s_ashr_i32 s21, s20, 31
	s_lshl_b64 s[20:21], s[20:21], 11
	v_lshl_add_u64 v[36:37], v[14:15], 0, s[20:21]
	v_readlane_b32 s20, v2, 3
	s_ashr_i32 s21, s20, 31
	s_lshl_b64 s[20:21], s[20:21], 11
	v_lshl_add_u64 v[38:39], v[14:15], 0, s[20:21]
	v_readlane_b32 s20, v2, 4
	s_ashr_i32 s5, s4, 31
	s_ashr_i32 s21, s20, 31
	s_lshl_b64 s[4:5], s[4:5], 12
	s_lshl_b64 s[20:21], s[20:21], 11
	v_lshl_add_u64 v[12:13], v[16:17], 0, s[4:5]
	v_lshl_add_u64 v[28:29], v[18:19], 0, s[4:5]
	global_load_dwordx2 v[32:33], v[30:31], off
	global_load_dwordx2 v[98:99], v[34:35], off
	global_load_dwordx2 v[62:63], v[36:37], off
	global_load_dwordx2 v[68:69], v[38:39], off
	v_lshl_add_u64 v[40:41], v[14:15], 0, s[20:21]
	v_readlane_b32 s20, v2, 5
	global_load_dwordx4 v[76:79], v[12:13], off
	global_load_dwordx4 v[94:97], v[28:29], off
	s_ashr_i32 s21, s20, 31
	s_lshl_b64 s[20:21], s[20:21], 11
	v_lshl_add_u64 v[42:43], v[14:15], 0, s[20:21]
	v_readlane_b32 s20, v2, 6
	s_ashr_i32 s21, s20, 31
	global_load_dwordx2 v[70:71], v[40:41], off
	global_load_dwordx2 v[72:73], v[42:43], off
	s_lshl_b64 s[20:21], s[20:21], 11
	v_lshl_add_u64 v[44:45], v[14:15], 0, s[20:21]
	global_load_dwordx2 v[74:75], v[44:45], off
	v_readlane_b32 s20, v2, 7
	s_ashr_i32 s21, s20, 31
	s_lshl_b64 s[20:21], s[20:21], 11
	v_lshl_add_u64 v[46:47], v[14:15], 0, s[20:21]
	global_load_dwordx2 v[88:89], v[46:47], off
	global_load_dwordx4 v[4:7], v[12:13], off offset:1024
	global_load_dwordx4 v[8:11], v[28:29], off offset:1024
	global_load_dwordx2 v[66:67], v[30:31], off offset:512
	global_load_dwordx2 v[64:65], v[34:35], off offset:512
	global_load_dwordx2 v[60:61], v[36:37], off offset:512
	global_load_dwordx2 v[56:57], v[38:39], off offset:512
	global_load_dwordx2 v[54:55], v[40:41], off offset:512
	global_load_dwordx2 v[52:53], v[42:43], off offset:512
	global_load_dwordx2 v[50:51], v[44:45], off offset:512
	global_load_dwordx2 v[48:49], v[46:47], off offset:512
	v_readlane_b32 s5, v1, 0
	s_mov_b32 s4, 0
	s_waitcnt vmcnt(10) lgkmcnt(0)
	v_cvt_pk_f32_fp8_e32 v[112:113], v32
	v_cvt_pk_f32_fp8_sdwa v[100:101], v32 src0_sel:WORD_1
	v_cvt_pk_f32_fp8_e32 v[114:115], v98
	v_cvt_pk_f32_fp8_sdwa v[116:117], v98 src0_sel:WORD_1
	v_cvt_pk_f32_fp8_e32 v[118:119], v99
	v_cvt_pk_f32_fp8_sdwa v[98:99], v99 src0_sel:WORD_1
	v_lshlrev_b32_e32 v90, 16, v76
	v_lshlrev_b32_e32 v92, 16, v94
	v_and_b32_e32 v91, 0xffff0000, v76
	v_and_b32_e32 v93, 0xffff0000, v94
	v_lshlrev_b32_e32 v84, 16, v77
	v_lshlrev_b32_e32 v86, 16, v95
	v_and_b32_e32 v85, 0xffff0000, v77
	v_and_b32_e32 v87, 0xffff0000, v95
	v_lshlrev_b32_e32 v80, 16, v78
	v_lshlrev_b32_e32 v82, 16, v96
	v_and_b32_e32 v81, 0xffff0000, v78
	v_and_b32_e32 v83, 0xffff0000, v96
	v_lshlrev_b32_e32 v76, 16, v79
	v_lshlrev_b32_e32 v78, 16, v97
	v_and_b32_e32 v77, 0xffff0000, v79
	v_and_b32_e32 v79, 0xffff0000, v97
	v_cvt_pk_f32_fp8_e32 v[96:97], v33
	v_cvt_pk_f32_fp8_sdwa v[94:95], v33 src0_sel:WORD_1
	v_cvt_pk_f32_fp8_e32 v[120:121], v62
	v_cvt_pk_f32_fp8_sdwa v[122:123], v62 src0_sel:WORD_1
	v_mul_f32_e32 v2, s5, v225
	v_readlane_b32 s5, v1, 1
	v_cvt_pk_f32_fp8_e32 v[124:125], v63
	v_cvt_pk_f32_fp8_sdwa v[126:127], v63 src0_sel:WORD_1
	v_cvt_pk_f32_fp8_e32 v[128:129], v68
	v_cvt_pk_f32_fp8_e32 v[160:161], v88
	v_cvt_pk_f32_fp8_sdwa v[162:163], v88 src0_sel:WORD_1
	v_cvt_pk_f32_fp8_e32 v[164:165], v89
	v_cvt_pk_f32_fp8_sdwa v[166:167], v89 src0_sel:WORD_1
	v_pk_fma_f32 v[88:89], v[90:91], s[96:97], v[92:93] op_sel_hi:[1,0,1]
	v_pk_fma_f32 v[84:85], v[84:85], s[96:97], v[86:87] op_sel_hi:[1,0,1]
	v_mul_f32_e32 v32, s5, v225
	v_readlane_b32 s5, v1, 2
	v_cvt_pk_f32_fp8_sdwa v[130:131], v68 src0_sel:WORD_1
	v_cvt_pk_f32_fp8_e32 v[132:133], v69
	v_cvt_pk_f32_fp8_sdwa v[134:135], v69 src0_sel:WORD_1
	v_pk_fma_f32 v[88:89], v[2:3], v[112:113], v[88:89] op_sel_hi:[0,1,1]
	v_pk_fma_f32 v[84:85], v[2:3], v[100:101], v[84:85] op_sel_hi:[0,1,1]
	v_pk_fma_f32 v[80:81], v[80:81], s[96:97], v[82:83] op_sel_hi:[1,0,1]
	v_pk_fma_f32 v[76:77], v[76:77], s[96:97], v[78:79] op_sel_hi:[1,0,1]
	v_mul_f32_e32 v58, s5, v225
	v_readlane_b32 s5, v1, 3
	v_cvt_pk_f32_fp8_e32 v[136:137], v70
	v_cvt_pk_f32_fp8_sdwa v[138:139], v70 src0_sel:WORD_1
	v_cvt_pk_f32_fp8_e32 v[140:141], v71
	v_pk_fma_f32 v[88:89], v[32:33], v[114:115], v[88:89] op_sel_hi:[0,1,1]
	v_pk_fma_f32 v[84:85], v[32:33], v[116:117], v[84:85] op_sel_hi:[0,1,1]
	v_pk_fma_f32 v[80:81], v[2:3], v[96:97], v[80:81] op_sel_hi:[0,1,1]
	v_pk_fma_f32 v[76:77], v[2:3], v[94:95], v[76:77] op_sel_hi:[0,1,1]
	v_mul_f32_e32 v62, s5, v225
	v_cvt_pk_f32_fp8_sdwa v[142:143], v71 src0_sel:WORD_1
	v_cvt_pk_f32_fp8_e32 v[144:145], v72
	v_cvt_pk_f32_fp8_sdwa v[146:147], v72 src0_sel:WORD_1
	v_pk_fma_f32 v[88:89], v[58:59], v[120:121], v[88:89] op_sel_hi:[0,1,1]
	v_pk_fma_f32 v[84:85], v[58:59], v[122:123], v[84:85] op_sel_hi:[0,1,1]
	v_pk_fma_f32 v[80:81], v[32:33], v[118:119], v[80:81] op_sel_hi:[0,1,1]
	v_pk_fma_f32 v[76:77], v[32:33], v[98:99], v[76:77] op_sel_hi:[0,1,1]
	s_waitcnt vmcnt(0)
	v_lshlrev_b32_e32 v120, 16, v10
	v_and_b32_e32 v121, 0xffff0000, v10
	v_lshlrev_b32_e32 v122, 16, v11
	v_and_b32_e32 v123, 0xffff0000, v11
	v_cvt_pk_f32_fp8_sdwa v[10:11], v66 src0_sel:WORD_1
	v_readlane_b32 s5, v1, 4
	v_cvt_pk_f32_fp8_e32 v[148:149], v73
	v_cvt_pk_f32_fp8_sdwa v[150:151], v73 src0_sel:WORD_1
	v_cvt_pk_f32_fp8_e32 v[152:153], v74
	v_pk_fma_f32 v[88:89], v[62:63], v[128:129], v[88:89] op_sel_hi:[0,1,1]
	v_pk_fma_f32 v[80:81], v[58:59], v[124:125], v[80:81] op_sel_hi:[0,1,1]
	v_pk_fma_f32 v[76:77], v[58:59], v[126:127], v[76:77] op_sel_hi:[0,1,1]
	v_cvt_pk_f32_fp8_sdwa v[128:129], v64 src0_sel:WORD_1
	v_mul_f32_e32 v68, s5, v225
	v_readlane_b32 s5, v1, 5
	v_cvt_pk_f32_fp8_e32 v[156:157], v75
	v_cvt_pk_f32_fp8_sdwa v[158:159], v75 src0_sel:WORD_1
	v_pk_fma_f32 v[84:85], v[62:63], v[130:131], v[84:85] op_sel_hi:[0,1,1]
	v_pk_fma_f32 v[80:81], v[62:63], v[132:133], v[80:81] op_sel_hi:[0,1,1]
	v_pk_fma_f32 v[76:77], v[62:63], v[134:135], v[76:77] op_sel_hi:[0,1,1]
	v_lshlrev_b32_e32 v112, 16, v4
	v_and_b32_e32 v113, 0xffff0000, v4
	v_lshlrev_b32_e32 v4, 16, v5
	v_lshlrev_b32_e32 v116, 16, v9
	v_and_b32_e32 v5, 0xffff0000, v5
	v_and_b32_e32 v117, 0xffff0000, v9
	v_cvt_pk_f32_fp8_sdwa v[134:135], v60 src0_sel:WORD_1
	v_mul_f32_e32 v70, s5, v225
	v_readlane_b32 s5, v1, 6
	v_pk_fma_f32 v[88:89], v[68:69], v[136:137], v[88:89] op_sel_hi:[0,1,1]
	v_pk_fma_f32 v[84:85], v[68:69], v[138:139], v[84:85] op_sel_hi:[0,1,1]
	v_pk_fma_f32 v[80:81], v[68:69], v[140:141], v[80:81] op_sel_hi:[0,1,1]
	v_cvt_pk_f32_fp8_sdwa v[140:141], v56 src0_sel:WORD_1
	v_pk_fma_f32 v[4:5], v[4:5], s[96:97], v[116:117] op_sel_hi:[1,0,1]
	v_mul_f32_e32 v72, s5, v225
	v_pk_fma_f32 v[88:89], v[70:71], v[144:145], v[88:89] op_sel_hi:[0,1,1]
	v_pk_fma_f32 v[84:85], v[70:71], v[146:147], v[84:85] op_sel_hi:[0,1,1]
	v_pk_fma_f32 v[76:77], v[68:69], v[142:143], v[76:77] op_sel_hi:[0,1,1]
	v_cvt_pk_f32_fp8_sdwa v[146:147], v54 src0_sel:WORD_1
	v_pk_fma_f32 v[4:5], v[2:3], v[10:11], v[4:5] op_sel_hi:[0,1,1]
	v_readlane_b32 s5, v1, 7
	v_pk_fma_f32 v[88:89], v[72:73], v[152:153], v[88:89] op_sel_hi:[0,1,1]
	v_pk_fma_f32 v[80:81], v[70:71], v[148:149], v[80:81] op_sel_hi:[0,1,1]
	v_pk_fma_f32 v[76:77], v[70:71], v[150:151], v[76:77] op_sel_hi:[0,1,1]
	v_cvt_pk_f32_fp8_sdwa v[152:153], v52 src0_sel:WORD_1
	v_pk_fma_f32 v[4:5], v[32:33], v[128:129], v[4:5] op_sel_hi:[0,1,1]
	v_cvt_pk_f32_fp8_sdwa v[154:155], v74 src0_sel:WORD_1
	v_mul_f32_e32 v74, s5, v225
	v_pk_fma_f32 v[80:81], v[72:73], v[156:157], v[80:81] op_sel_hi:[0,1,1]
	v_pk_fma_f32 v[76:77], v[72:73], v[158:159], v[76:77] op_sel_hi:[0,1,1]
	v_cvt_pk_f32_fp8_sdwa v[158:159], v50 src0_sel:WORD_1
	v_pk_fma_f32 v[4:5], v[58:59], v[134:135], v[4:5] op_sel_hi:[0,1,1]
	v_pk_fma_f32 v[80:81], v[74:75], v[164:165], v[80:81] op_sel_hi:[0,1,1]
	v_cvt_pk_f32_fp8_sdwa v[164:165], v48 src0_sel:WORD_1
	v_pk_fma_f32 v[4:5], v[62:63], v[140:141], v[4:5] op_sel_hi:[0,1,1]
	v_cvt_pk_f32_fp8_e32 v[124:125], v67
	v_pk_fma_f32 v[4:5], v[68:69], v[146:147], v[4:5] op_sel_hi:[0,1,1]
	v_cvt_pk_f32_fp8_e32 v[130:131], v65
	v_pk_fma_f32 v[4:5], v[70:71], v[152:153], v[4:5] op_sel_hi:[0,1,1]
	v_lshlrev_b32_e32 v118, 16, v6
	v_and_b32_e32 v119, 0xffff0000, v6
	v_cvt_pk_f32_fp8_e32 v[136:137], v61
	v_pk_fma_f32 v[4:5], v[72:73], v[158:159], v[4:5] op_sel_hi:[0,1,1]
	v_cvt_pk_f32_fp8_e32 v[142:143], v57
	v_pk_fma_f32 v[10:11], v[74:75], v[164:165], v[4:5] op_sel_hi:[0,1,1]
	v_pk_fma_f32 v[4:5], v[118:119], s[96:97], v[120:121] op_sel_hi:[1,0,1]
	v_cvt_pk_f32_fp8_e32 v[148:149], v55
	v_pk_fma_f32 v[4:5], v[2:3], v[124:125], v[4:5] op_sel_hi:[0,1,1]
	v_pk_fma_f32 v[88:89], v[74:75], v[160:161], v[88:89] op_sel_hi:[0,1,1]
	v_pk_fma_f32 v[84:85], v[72:73], v[154:155], v[84:85] op_sel_hi:[0,1,1]
	v_cvt_pk_f32_fp8_e32 v[154:155], v53
	v_pk_fma_f32 v[4:5], v[32:33], v[130:131], v[4:5] op_sel_hi:[0,1,1]
	v_pk_fma_f32 v[90:91], v[74:75], v[162:163], v[84:85] op_sel_hi:[0,1,1]
	v_pk_fma_f32 v[82:83], v[74:75], v[166:167], v[76:77] op_sel_hi:[0,1,1]
	v_mov_b32_e32 v76, v88
	v_mov_b32_e32 v77, v80
	v_mov_b32_e32 v78, v89
	v_mov_b32_e32 v79, v81
	v_cvt_pk_f32_fp8_e32 v[160:161], v51
	v_pk_fma_f32 v[4:5], v[58:59], v[136:137], v[4:5] op_sel_hi:[0,1,1]
	v_pk_add_f32 v[76:77], v[76:77], v[78:79]
	v_mov_b32_e32 v78, v90
	v_mov_b32_e32 v79, v82
	v_mov_b32_e32 v84, v91
	v_mov_b32_e32 v85, v83
	v_lshlrev_b32_e32 v114, 16, v8
	v_and_b32_e32 v115, 0xffff0000, v8
	v_cvt_pk_f32_fp8_e32 v[8:9], v66
	v_cvt_pk_f32_fp8_e32 v[166:167], v49
	v_pk_fma_f32 v[4:5], v[62:63], v[142:143], v[4:5] op_sel_hi:[0,1,1]
	v_pk_add_f32 v[78:79], v[78:79], v[84:85]
	ds_write_b128 v103, v[88:91]
	ds_write_b128 v103, v[80:83] offset:16
	v_cvt_pk_f32_fp8_sdwa v[66:67], v67 src0_sel:WORD_1
	v_cvt_pk_f32_fp8_e32 v[126:127], v64
	v_pk_fma_f32 v[4:5], v[68:69], v[148:149], v[4:5] op_sel_hi:[0,1,1]
	v_pk_add_f32 v[76:77], v[76:77], v[78:79]
	global_load_dwordx4 v[78:81], v[12:13], off offset:2048
	global_load_dwordx4 v[82:85], v[28:29], off offset:2048
	global_load_dwordx2 v[86:87], v[30:31], off offset:1024
	global_load_dwordx2 v[88:89], v[34:35], off offset:1024
	global_load_dwordx2 v[90:91], v[36:37], off offset:1024
	global_load_dwordx2 v[92:93], v[38:39], off offset:1024
	global_load_dwordx2 v[94:95], v[40:41], off offset:1024
	global_load_dwordx2 v[96:97], v[42:43], off offset:1024
	global_load_dwordx2 v[98:99], v[44:45], off offset:1024
	global_load_dwordx2 v[100:101], v[46:47], off offset:1024
	v_cvt_pk_f32_fp8_sdwa v[64:65], v65 src0_sel:WORD_1
	v_cvt_pk_f32_fp8_e32 v[132:133], v60
	v_pk_fma_f32 v[4:5], v[70:71], v[154:155], v[4:5] op_sel_hi:[0,1,1]
	v_lshlrev_b32_e32 v6, 16, v7
	v_and_b32_e32 v7, 0xffff0000, v7
	v_cvt_pk_f32_fp8_sdwa v[60:61], v61 src0_sel:WORD_1
	v_cvt_pk_f32_fp8_e32 v[138:139], v56
	v_cvt_pk_f32_fp8_e32 v[162:163], v48
	v_cvt_pk_f32_fp8_sdwa v[168:169], v49 src0_sel:WORD_1
	v_pk_fma_f32 v[48:49], v[112:113], s[96:97], v[114:115] op_sel_hi:[1,0,1]
	v_pk_fma_f32 v[4:5], v[72:73], v[160:161], v[4:5] op_sel_hi:[0,1,1]
	v_cvt_pk_f32_fp8_sdwa v[56:57], v57 src0_sel:WORD_1
	v_cvt_pk_f32_fp8_e32 v[144:145], v54
	v_pk_fma_f32 v[8:9], v[2:3], v[8:9], v[48:49] op_sel_hi:[0,1,1]
	v_pk_fma_f32 v[48:49], v[74:75], v[166:167], v[4:5] op_sel_hi:[0,1,1]
	v_pk_fma_f32 v[4:5], v[6:7], s[96:97], v[122:123] op_sel_hi:[1,0,1]
	v_cvt_pk_f32_fp8_sdwa v[54:55], v55 src0_sel:WORD_1
	v_cvt_pk_f32_fp8_e32 v[150:151], v52
	v_pk_fma_f32 v[8:9], v[32:33], v[126:127], v[8:9] op_sel_hi:[0,1,1]
	v_pk_fma_f32 v[4:5], v[2:3], v[66:67], v[4:5] op_sel_hi:[0,1,1]
	v_cvt_pk_f32_fp8_sdwa v[52:53], v53 src0_sel:WORD_1
	v_cvt_pk_f32_fp8_e32 v[156:157], v50
	v_pk_fma_f32 v[8:9], v[58:59], v[132:133], v[8:9] op_sel_hi:[0,1,1]
	v_pk_fma_f32 v[4:5], v[32:33], v[64:65], v[4:5] op_sel_hi:[0,1,1]
	v_cvt_pk_f32_fp8_sdwa v[50:51], v51 src0_sel:WORD_1
	v_pk_fma_f32 v[8:9], v[62:63], v[138:139], v[8:9] op_sel_hi:[0,1,1]
	v_pk_fma_f32 v[4:5], v[58:59], v[60:61], v[4:5] op_sel_hi:[0,1,1]
	v_pk_fma_f32 v[8:9], v[68:69], v[144:145], v[8:9] op_sel_hi:[0,1,1]
	v_pk_fma_f32 v[4:5], v[62:63], v[56:57], v[4:5] op_sel_hi:[0,1,1]
	v_pk_fma_f32 v[8:9], v[70:71], v[150:151], v[8:9] op_sel_hi:[0,1,1]
	v_pk_fma_f32 v[4:5], v[68:69], v[54:55], v[4:5] op_sel_hi:[0,1,1]
	v_pk_fma_f32 v[8:9], v[72:73], v[156:157], v[8:9] op_sel_hi:[0,1,1]
	v_pk_fma_f32 v[4:5], v[70:71], v[52:53], v[4:5] op_sel_hi:[0,1,1]
	v_pk_fma_f32 v[8:9], v[74:75], v[162:163], v[8:9] op_sel_hi:[0,1,1]
	v_pk_fma_f32 v[4:5], v[72:73], v[50:51], v[4:5] op_sel_hi:[0,1,1]
	v_pk_fma_f32 v[50:51], v[74:75], v[168:169], v[4:5] op_sel_hi:[0,1,1]
	v_mov_b32_e32 v4, v8
	v_mov_b32_e32 v5, v10
	v_mov_b32_e32 v6, v9
	v_mov_b32_e32 v7, v11
	v_pk_add_f32 v[4:5], v[4:5], v[6:7]
	v_mov_b32_e32 v6, v48
	v_mov_b32_e32 v7, v50
	v_mov_b32_e32 v52, v49
	v_mov_b32_e32 v53, v51
	ds_write_b128 v103, v[8:11] offset:2048
	ds_write_b128 v103, v[48:51] offset:2064
	v_pk_add_f32 v[6:7], v[6:7], v[52:53]
	global_load_dwordx4 v[8:11], v[12:13], off offset:3072
	global_load_dwordx4 v[48:51], v[28:29], off offset:3072
	s_nop 0
	global_load_dwordx2 v[12:13], v[30:31], off offset:1536
	global_load_dwordx2 v[52:53], v[34:35], off offset:1536
	global_load_dwordx2 v[54:55], v[36:37], off offset:1536
	s_nop 0
	global_load_dwordx2 v[38:39], v[38:39], off offset:1536
	s_nop 0
	global_load_dwordx2 v[40:41], v[40:41], off offset:1536
	s_nop 0
	global_load_dwordx2 v[42:43], v[42:43], off offset:1536
	s_nop 0
	global_load_dwordx2 v[44:45], v[44:45], off offset:1536
	s_nop 0
	global_load_dwordx2 v[46:47], v[46:47], off offset:1536
	v_pk_add_f32 v[76:77], v[76:77], v[76:77] op_sel:[0,1] op_sel_hi:[1,0]
	v_pk_add_f32 v[4:5], v[4:5], v[4:5] op_sel:[0,1] op_sel_hi:[1,0]
	v_pk_add_f32 v[6:7], v[6:7], v[6:7] op_sel:[0,1] op_sel_hi:[1,0]
	s_waitcnt vmcnt(10) lgkmcnt(0)
	v_lshlrev_b32_e32 v28, 16, v78
	v_lshlrev_b32_e32 v30, 16, v82
	v_and_b32_e32 v29, 0xffff0000, v78
	v_and_b32_e32 v31, 0xffff0000, v82
	v_lshlrev_b32_e32 v34, 16, v79
	v_lshlrev_b32_e32 v36, 16, v83
	v_and_b32_e32 v35, 0xffff0000, v79
	v_and_b32_e32 v37, 0xffff0000, v83
	v_lshlrev_b32_e32 v56, 16, v80
	v_and_b32_e32 v57, 0xffff0000, v80
	v_lshlrev_b32_e32 v64, 16, v81
	v_and_b32_e32 v65, 0xffff0000, v81
	v_cvt_pk_f32_fp8_e32 v[78:79], v86
	v_cvt_pk_f32_fp8_sdwa v[80:81], v86 src0_sel:WORD_1
	v_cvt_pk_f32_fp8_e32 v[82:83], v87
	v_lshlrev_b32_e32 v60, 16, v84
	v_and_b32_e32 v61, 0xffff0000, v84
	v_lshlrev_b32_e32 v66, 16, v85
	v_and_b32_e32 v67, 0xffff0000, v85
	v_cvt_pk_f32_fp8_sdwa v[84:85], v87 src0_sel:WORD_1
	v_cvt_pk_f32_fp8_e32 v[86:87], v88
	v_cvt_pk_f32_fp8_sdwa v[112:113], v88 src0_sel:WORD_1
	v_cvt_pk_f32_fp8_e32 v[114:115], v89
	v_cvt_pk_f32_fp8_sdwa v[88:89], v89 src0_sel:WORD_1
	v_cvt_pk_f32_fp8_e32 v[116:117], v90
	v_cvt_pk_f32_fp8_sdwa v[118:119], v90 src0_sel:WORD_1
	v_cvt_pk_f32_fp8_e32 v[120:121], v91
	v_cvt_pk_f32_fp8_sdwa v[90:91], v91 src0_sel:WORD_1
	v_cvt_pk_f32_fp8_e32 v[122:123], v92
	v_cvt_pk_f32_fp8_sdwa v[124:125], v92 src0_sel:WORD_1
	v_cvt_pk_f32_fp8_e32 v[126:127], v93
	v_pk_fma_f32 v[28:29], v[28:29], s[96:97], v[30:31] op_sel_hi:[1,0,1]
	v_pk_fma_f32 v[30:31], v[34:35], s[96:97], v[36:37] op_sel_hi:[1,0,1]
	v_pk_fma_f32 v[34:35], v[56:57], s[96:97], v[60:61] op_sel_hi:[1,0,1]
	v_cvt_pk_f32_fp8_sdwa v[92:93], v93 src0_sel:WORD_1
	v_cvt_pk_f32_fp8_e32 v[128:129], v94
	v_cvt_pk_f32_fp8_sdwa v[130:131], v94 src0_sel:WORD_1
	v_cvt_pk_f32_fp8_e32 v[132:133], v95
	v_pk_fma_f32 v[28:29], v[2:3], v[78:79], v[28:29] op_sel_hi:[0,1,1]
	v_pk_fma_f32 v[30:31], v[2:3], v[80:81], v[30:31] op_sel_hi:[0,1,1]
	v_pk_fma_f32 v[34:35], v[2:3], v[82:83], v[34:35] op_sel_hi:[0,1,1]
	v_pk_fma_f32 v[36:37], v[64:65], s[96:97], v[66:67] op_sel_hi:[1,0,1]
	v_cvt_pk_f32_fp8_sdwa v[94:95], v95 src0_sel:WORD_1
	v_cvt_pk_f32_fp8_e32 v[134:135], v96
	v_cvt_pk_f32_fp8_sdwa v[136:137], v96 src0_sel:WORD_1
	v_cvt_pk_f32_fp8_e32 v[138:139], v97
	v_pk_fma_f32 v[28:29], v[32:33], v[86:87], v[28:29] op_sel_hi:[0,1,1]
	v_pk_fma_f32 v[30:31], v[32:33], v[112:113], v[30:31] op_sel_hi:[0,1,1]
	v_pk_fma_f32 v[34:35], v[32:33], v[114:115], v[34:35] op_sel_hi:[0,1,1]
	v_pk_fma_f32 v[36:37], v[2:3], v[84:85], v[36:37] op_sel_hi:[0,1,1]
	v_cvt_pk_f32_fp8_sdwa v[96:97], v97 src0_sel:WORD_1
	v_cvt_pk_f32_fp8_e32 v[140:141], v98
	v_cvt_pk_f32_fp8_sdwa v[142:143], v98 src0_sel:WORD_1
	v_cvt_pk_f32_fp8_e32 v[144:145], v99
	v_pk_fma_f32 v[28:29], v[58:59], v[116:117], v[28:29] op_sel_hi:[0,1,1]
	v_pk_fma_f32 v[30:31], v[58:59], v[118:119], v[30:31] op_sel_hi:[0,1,1]
	v_pk_fma_f32 v[34:35], v[58:59], v[120:121], v[34:35] op_sel_hi:[0,1,1]
	v_pk_fma_f32 v[36:37], v[32:33], v[88:89], v[36:37] op_sel_hi:[0,1,1]
	v_cvt_pk_f32_fp8_sdwa v[98:99], v99 src0_sel:WORD_1
	v_cvt_pk_f32_fp8_e32 v[146:147], v100
	v_cvt_pk_f32_fp8_sdwa v[148:149], v100 src0_sel:WORD_1
	v_cvt_pk_f32_fp8_e32 v[150:151], v101
	v_pk_fma_f32 v[28:29], v[62:63], v[122:123], v[28:29] op_sel_hi:[0,1,1]
	v_pk_fma_f32 v[30:31], v[62:63], v[124:125], v[30:31] op_sel_hi:[0,1,1]
	v_pk_fma_f32 v[34:35], v[62:63], v[126:127], v[34:35] op_sel_hi:[0,1,1]
	v_pk_fma_f32 v[36:37], v[58:59], v[90:91], v[36:37] op_sel_hi:[0,1,1]
	v_cvt_pk_f32_fp8_sdwa v[100:101], v101 src0_sel:WORD_1
	v_pk_fma_f32 v[28:29], v[68:69], v[128:129], v[28:29] op_sel_hi:[0,1,1]
	v_pk_fma_f32 v[30:31], v[68:69], v[130:131], v[30:31] op_sel_hi:[0,1,1]
	v_pk_fma_f32 v[34:35], v[68:69], v[132:133], v[34:35] op_sel_hi:[0,1,1]
	v_pk_fma_f32 v[36:37], v[62:63], v[92:93], v[36:37] op_sel_hi:[0,1,1]
	v_pk_fma_f32 v[28:29], v[70:71], v[134:135], v[28:29] op_sel_hi:[0,1,1]
	v_pk_fma_f32 v[30:31], v[70:71], v[136:137], v[30:31] op_sel_hi:[0,1,1]
	v_pk_fma_f32 v[34:35], v[70:71], v[138:139], v[34:35] op_sel_hi:[0,1,1]
	v_pk_fma_f32 v[36:37], v[68:69], v[94:95], v[36:37] op_sel_hi:[0,1,1]
	v_pk_fma_f32 v[28:29], v[72:73], v[140:141], v[28:29] op_sel_hi:[0,1,1]
	v_pk_fma_f32 v[30:31], v[72:73], v[142:143], v[30:31] op_sel_hi:[0,1,1]
	v_pk_fma_f32 v[34:35], v[72:73], v[144:145], v[34:35] op_sel_hi:[0,1,1]
	v_pk_fma_f32 v[36:37], v[70:71], v[96:97], v[36:37] op_sel_hi:[0,1,1]
	v_pk_fma_f32 v[28:29], v[74:75], v[146:147], v[28:29] op_sel_hi:[0,1,1]
	v_pk_fma_f32 v[30:31], v[74:75], v[148:149], v[30:31] op_sel_hi:[0,1,1]
	v_pk_fma_f32 v[34:35], v[74:75], v[150:151], v[34:35] op_sel_hi:[0,1,1]
	v_pk_fma_f32 v[36:37], v[72:73], v[98:99], v[36:37] op_sel_hi:[0,1,1]
	v_pk_fma_f32 v[36:37], v[74:75], v[100:101], v[36:37] op_sel_hi:[0,1,1]
	v_pk_add_f32 v[56:57], v[28:29], v[28:29] op_sel:[1,0] op_sel_hi:[0,1]
	v_pk_add_f32 v[64:65], v[34:35], v[34:35] op_sel:[1,0] op_sel_hi:[0,1]
	ds_write_b128 v103, v[28:31] offset:4096
	ds_write_b128 v103, v[34:37] offset:4112
	s_waitcnt vmcnt(0)
	v_lshlrev_b32_e32 v28, 16, v8
	v_and_b32_e32 v29, 0xffff0000, v8
	v_lshlrev_b32_e32 v34, 16, v9
	v_and_b32_e32 v35, 0xffff0000, v9
	v_cvt_pk_f32_fp8_e32 v[8:9], v12
	v_pk_add_f32 v[60:61], v[30:31], v[30:31] op_sel:[1,0] op_sel_hi:[0,1]
	v_pk_add_f32 v[66:67], v[36:37], v[36:37] op_sel:[1,0] op_sel_hi:[0,1]
	v_lshlrev_b32_e32 v30, 16, v48
	v_and_b32_e32 v31, 0xffff0000, v48
	v_lshlrev_b32_e32 v36, 16, v49
	v_and_b32_e32 v37, 0xffff0000, v49
	v_lshlrev_b32_e32 v48, 16, v10
	v_and_b32_e32 v49, 0xffff0000, v10
	v_lshlrev_b32_e32 v80, 16, v11
	v_and_b32_e32 v81, 0xffff0000, v11
	v_cvt_pk_f32_fp8_sdwa v[10:11], v12 src0_sel:WORD_1
	v_cvt_pk_f32_fp8_e32 v[82:83], v13
	v_cvt_pk_f32_fp8_sdwa v[12:13], v13 src0_sel:WORD_1
	v_cvt_pk_f32_fp8_e32 v[84:85], v52
	v_cvt_pk_f32_fp8_sdwa v[86:87], v52 src0_sel:WORD_1
	v_cvt_pk_f32_fp8_e32 v[88:89], v53
	v_cvt_pk_f32_fp8_sdwa v[52:53], v53 src0_sel:WORD_1
	v_cvt_pk_f32_fp8_e32 v[90:91], v54
	v_cvt_pk_f32_fp8_sdwa v[92:93], v54 src0_sel:WORD_1
	v_pk_fma_f32 v[28:29], v[28:29], s[96:97], v[30:31] op_sel_hi:[1,0,1]
	v_lshlrev_b32_e32 v78, 16, v50
	v_and_b32_e32 v79, 0xffff0000, v50
	v_lshlrev_b32_e32 v50, 16, v51
	v_and_b32_e32 v51, 0xffff0000, v51
	v_cvt_pk_f32_fp8_e32 v[94:95], v55
	v_cvt_pk_f32_fp8_sdwa v[54:55], v55 src0_sel:WORD_1
	v_cvt_pk_f32_fp8_e32 v[96:97], v38
	v_cvt_pk_f32_fp8_sdwa v[98:99], v38 src0_sel:WORD_1
	v_pk_fma_f32 v[8:9], v[2:3], v[8:9], v[28:29] op_sel_hi:[0,1,1]
	v_pk_fma_f32 v[28:29], v[34:35], s[96:97], v[36:37] op_sel_hi:[1,0,1]
	v_cvt_pk_f32_fp8_e32 v[100:101], v39
	v_cvt_pk_f32_fp8_sdwa v[38:39], v39 src0_sel:WORD_1
	v_cvt_pk_f32_fp8_e32 v[112:113], v40
	v_cvt_pk_f32_fp8_sdwa v[114:115], v40 src0_sel:WORD_1
	v_pk_fma_f32 v[10:11], v[2:3], v[10:11], v[28:29] op_sel_hi:[0,1,1]
	v_pk_fma_f32 v[28:29], v[48:49], s[96:97], v[78:79] op_sel_hi:[1,0,1]
	v_pk_fma_f32 v[30:31], v[80:81], s[96:97], v[50:51] op_sel_hi:[1,0,1]
	v_cvt_pk_f32_fp8_e32 v[116:117], v41
	v_cvt_pk_f32_fp8_sdwa v[40:41], v41 src0_sel:WORD_1
	v_cvt_pk_f32_fp8_e32 v[118:119], v42
	v_cvt_pk_f32_fp8_sdwa v[120:121], v42 src0_sel:WORD_1
	v_pk_fma_f32 v[8:9], v[32:33], v[84:85], v[8:9] op_sel_hi:[0,1,1]
	v_pk_fma_f32 v[10:11], v[32:33], v[86:87], v[10:11] op_sel_hi:[0,1,1]
	v_pk_fma_f32 v[28:29], v[2:3], v[82:83], v[28:29] op_sel_hi:[0,1,1]
	v_pk_fma_f32 v[12:13], v[2:3], v[12:13], v[30:31] op_sel_hi:[0,1,1]
	v_cvt_pk_f32_fp8_e32 v[122:123], v43
	v_cvt_pk_f32_fp8_sdwa v[42:43], v43 src0_sel:WORD_1
	v_cvt_pk_f32_fp8_e32 v[124:125], v44
	v_cvt_pk_f32_fp8_sdwa v[126:127], v44 src0_sel:WORD_1
	v_pk_fma_f32 v[8:9], v[58:59], v[90:91], v[8:9] op_sel_hi:[0,1,1]
	v_pk_fma_f32 v[10:11], v[58:59], v[92:93], v[10:11] op_sel_hi:[0,1,1]
	v_pk_fma_f32 v[28:29], v[32:33], v[88:89], v[28:29] op_sel_hi:[0,1,1]
	v_pk_fma_f32 v[12:13], v[32:33], v[52:53], v[12:13] op_sel_hi:[0,1,1]
	v_cvt_pk_f32_fp8_e32 v[128:129], v45
	v_cvt_pk_f32_fp8_sdwa v[44:45], v45 src0_sel:WORD_1
	v_cvt_pk_f32_fp8_e32 v[130:131], v46
	v_cvt_pk_f32_fp8_sdwa v[132:133], v46 src0_sel:WORD_1
	v_pk_fma_f32 v[8:9], v[62:63], v[96:97], v[8:9] op_sel_hi:[0,1,1]
	v_pk_fma_f32 v[10:11], v[62:63], v[98:99], v[10:11] op_sel_hi:[0,1,1]
	v_pk_fma_f32 v[28:29], v[58:59], v[94:95], v[28:29] op_sel_hi:[0,1,1]
	v_pk_fma_f32 v[12:13], v[58:59], v[54:55], v[12:13] op_sel_hi:[0,1,1]
	v_cvt_pk_f32_fp8_e32 v[134:135], v47
	v_cvt_pk_f32_fp8_sdwa v[46:47], v47 src0_sel:WORD_1
	v_pk_fma_f32 v[8:9], v[68:69], v[112:113], v[8:9] op_sel_hi:[0,1,1]
	v_pk_fma_f32 v[10:11], v[68:69], v[114:115], v[10:11] op_sel_hi:[0,1,1]
	v_pk_fma_f32 v[28:29], v[62:63], v[100:101], v[28:29] op_sel_hi:[0,1,1]
	v_pk_fma_f32 v[12:13], v[62:63], v[38:39], v[12:13] op_sel_hi:[0,1,1]
	v_pk_fma_f32 v[8:9], v[70:71], v[118:119], v[8:9] op_sel_hi:[0,1,1]
	v_pk_fma_f32 v[10:11], v[70:71], v[120:121], v[10:11] op_sel_hi:[0,1,1]
	v_pk_fma_f32 v[28:29], v[68:69], v[116:117], v[28:29] op_sel_hi:[0,1,1]
	v_pk_fma_f32 v[12:13], v[68:69], v[40:41], v[12:13] op_sel_hi:[0,1,1]
	v_pk_fma_f32 v[8:9], v[72:73], v[124:125], v[8:9] op_sel_hi:[0,1,1]
	v_pk_fma_f32 v[10:11], v[72:73], v[126:127], v[10:11] op_sel_hi:[0,1,1]
	v_pk_fma_f32 v[28:29], v[70:71], v[122:123], v[28:29] op_sel_hi:[0,1,1]
	v_pk_fma_f32 v[12:13], v[70:71], v[42:43], v[12:13] op_sel_hi:[0,1,1]
	v_pk_fma_f32 v[8:9], v[74:75], v[130:131], v[8:9] op_sel_hi:[0,1,1]
	v_pk_fma_f32 v[10:11], v[74:75], v[132:133], v[10:11] op_sel_hi:[0,1,1]
	v_pk_fma_f32 v[28:29], v[72:73], v[128:129], v[28:29] op_sel_hi:[0,1,1]
	v_pk_fma_f32 v[12:13], v[72:73], v[44:45], v[12:13] op_sel_hi:[0,1,1]
	v_pk_fma_f32 v[28:29], v[74:75], v[134:135], v[28:29] op_sel_hi:[0,1,1]
	v_pk_fma_f32 v[30:31], v[74:75], v[46:47], v[12:13] op_sel_hi:[0,1,1]
	v_mov_b32_e32 v77, v9
	v_mov_b32_e32 v12, v3
	v_mov_b32_e32 v13, v8
	v_mov_b32_e32 v5, v11
	v_mov_b32_e32 v7, v10
	v_pk_add_f32 v[12:13], v[76:77], v[12:13]
	v_pk_add_f32 v[4:5], v[4:5], v[6:7]
	v_mov_b32_e32 v57, v29
	v_mov_b32_e32 v61, v28
	v_mov_b32_e32 v65, v31
	v_mov_b32_e32 v67, v30
	v_pk_add_f32 v[4:5], v[12:13], v[4:5]
	v_pk_add_f32 v[6:7], v[56:57], v[60:61]
	v_pk_add_f32 v[12:13], v[64:65], v[66:67]
	ds_write_b128 v103, v[8:11] offset:6144
	ds_write_b128 v103, v[28:31] offset:6160
	v_pk_add_f32 v[6:7], v[6:7], v[12:13]
	s_nop 0
	v_pk_add_f32 v[4:5], v[4:5], v[6:7]
	v_mov_b32_e32 v6, 0
	v_add_f32_e32 v1, v4, v5
	ds_bpermute_b32 v2, v104, v1
	s_waitcnt lgkmcnt(0)
	v_add_f32_e32 v1, v1, v2
	ds_bpermute_b32 v2, v105, v1
	s_waitcnt lgkmcnt(0)
	v_add_f32_e32 v1, v1, v2
	ds_bpermute_b32 v2, v106, v1
	s_waitcnt lgkmcnt(0)
	v_add_f32_e32 v1, v1, v2
	ds_bpermute_b32 v2, v107, v1
	s_waitcnt lgkmcnt(0)
	v_add_f32_e32 v1, v1, v2
	ds_bpermute_b32 v2, v108, v1
	s_waitcnt lgkmcnt(0)
	v_add_f32_e32 v1, v1, v2
	ds_bpermute_b32 v2, v109, v1
	s_waitcnt lgkmcnt(0)
	v_add_f32_e32 v1, v1, v2
	v_mul_f32_e32 v2, 0x3a000000, v1
	v_mov_b32_e32 v1, v2
	v_mov_b32_e32 v4, v2
	v_mov_b32_e32 v5, v2
